# hand-written norm2+router phase: 16B loads/stores, norm weights in registers, router weights in padded LDS, DPP reduce-scatter (plus v4 attention loop)
# speedup vs baseline: 1.0187x; 1.0155x over previous
.LBB0_1393:
	s_andn2_b64 vcc, exec, s[0:1]
	s_cbranch_vccnz .LBB0_1456
	s_waitcnt vmcnt(0) lgkmcnt(0)
	s_barrier
	s_load_dwordx2 s[34:35], s[76:77], 0x130
	s_load_dwordx2 s[36:37], s[76:77], 0x140
	s_load_dwordx2 s[38:39], s[76:77], 0x1c0
	s_load_dwordx2 s[40:41], s[76:77], 0x38
	s_load_dwordx2 s[42:43], s[76:77], 0x120
	s_load_dwordx2 s[44:45], s[76:77], 0xb0
	v_readlane_b32 s9, v254, 0
	v_and_b32_e32 v2, 63, v0
	v_lshrrev_b32_e32 v8, 6, v0
	s_nop 0
	v_readfirstlane_b32 s29, v8
	s_waitcnt lgkmcnt(0)
	s_lshl_b32 s0, s28, 16
	s_add_u32 s44, s44, s0
	s_addc_u32 s45, s45, 0
	s_lshl_b32 s0, s28, 12
	s_add_u32 s40, s40, s0
	s_addc_u32 s41, s41, 0
	s_mul_i32 s0, s28, 0x12000
	s_add_u32 s42, s42, s0
	s_addc_u32 s43, s43, 0
	v_lshlrev_b32_e32 v9, 4, v0
	v_lshrrev_b32_e32 v10, 6, v0
	v_mul_u32_u24_e32 v10, 0x410, v10
	v_bfe_u32 v11, v0, 2, 4
	v_lshl_add_u32 v10, v11, 6, v10
	v_and_b32_e32 v11, 3, v0
	v_lshl_add_u32 v10, v11, 4, v10
	s_mov_b64 s[14:15], s[44:45]
	global_load_dwordx4 v[144:147], v9, s[14:15]
	s_add_u32 s14, s14, 0x2000
	s_addc_u32 s15, s15, 0
	global_load_dwordx4 v[148:151], v9, s[14:15]
	s_add_u32 s14, s14, 0x2000
	s_addc_u32 s15, s15, 0
	global_load_dwordx4 v[152:155], v9, s[14:15]
	s_add_u32 s14, s14, 0x2000
	s_addc_u32 s15, s15, 0
	global_load_dwordx4 v[156:159], v9, s[14:15]
	s_add_u32 s14, s14, 0x2000
	s_addc_u32 s15, s15, 0
	global_load_dwordx4 v[160:163], v9, s[14:15]
	s_add_u32 s14, s14, 0x2000
	s_addc_u32 s15, s15, 0
	global_load_dwordx4 v[164:167], v9, s[14:15]
	s_add_u32 s14, s14, 0x2000
	s_addc_u32 s15, s15, 0
	global_load_dwordx4 v[168:171], v9, s[14:15]
	s_add_u32 s14, s14, 0x2000
	s_addc_u32 s15, s15, 0
	global_load_dwordx4 v[172:175], v9, s[14:15]
	s_waitcnt vmcnt(7)
	ds_write_b128 v10, v[144:147] offset:64
	s_waitcnt vmcnt(6)
	ds_write_b128 v10, v[148:151] offset:8384
	s_waitcnt vmcnt(5)
	ds_write_b128 v10, v[152:155] offset:16704
	s_waitcnt vmcnt(4)
	ds_write_b128 v10, v[156:159] offset:25024
	s_waitcnt vmcnt(3)
	ds_write_b128 v10, v[160:163] offset:33344
	s_waitcnt vmcnt(2)
	ds_write_b128 v10, v[164:167] offset:41664
	s_waitcnt vmcnt(1)
	ds_write_b128 v10, v[168:171] offset:49984
	s_waitcnt vmcnt(0)
	ds_write_b128 v10, v[172:175] offset:58304
	v_lshlrev_b32_e32 v3, 6, v2
	v_lshlrev_b32_e32 v4, 5, v2
	v_mul_u32_u24_e32 v7, 0x410, v2
	v_add_u32_e32 v7, 64, v7
	v_and_b32_e32 v9, 1, v2
	v_lshlrev_b32_e32 v9, 3, v9
	v_and_b32_e32 v10, 2, v2
	v_lshl_or_b32 v9, v10, 1, v9
	v_and_b32_e32 v10, 4, v2
	v_lshrrev_b32_e32 v10, 1, v10
	v_or_b32_e32 v9, v9, v10
	v_bfe_u32 v10, v2, 3, 1
	v_or_b32_e32 v9, v9, v10
	v_lshlrev_b32_e32 v5, 15, v9
	v_lshlrev_b32_e32 v6, 10, v9
	s_mov_b32 s58, 0xaaaaaaaa
	s_mov_b32 s59, 0xaaaaaaaa
	s_mov_b32 s60, 0xcccccccc
	s_mov_b32 s61, 0xcccccccc
	s_mov_b32 s62, 0xf0f0f0f0
	s_mov_b32 s63, 0xf0f0f0f0
	s_mov_b32 s64, 0xff00ff00
	s_mov_b32 s65, 0xff00ff00
	s_mov_b32 s66, 0xffff
	s_mov_b32 s67, 0
	s_lshl_b32 s9, s9, 3
	s_add_i32 s9, s9, s29
	s_cmp_eq_u32 s28, 3
	s_cselect_b32 s0, 32, 33
	s_mul_i32 s46, s9, s0
	s_add_i32 s47, s46, s0
	s_lshr_b32 s46, s46, 2
	s_lshr_b32 s47, s47, 2
	s_mov_b32 s48, -1
	s_lshl_b32 s0, s46, 12
	s_add_u32 s50, s34, s0
	s_addc_u32 s51, s35, 0
	global_load_dwordx4 v[16:19], v3, s[50:51] offset:0
	global_load_dwordx4 v[20:23], v3, s[50:51] offset:16
	global_load_dwordx4 v[24:27], v3, s[50:51] offset:32
	global_load_dwordx4 v[28:31], v3, s[50:51] offset:48
	s_waitcnt lgkmcnt(0)
	s_barrier
.Ln2_row:
	s_lshr_b32 s0, s46, 13
	s_cmp_eq_u32 s0, s48
	s_cbranch_scc1 .Ln2_wa_ok
	s_mov_b32 s48, s0
	s_mul_i32 s0, s48, 0x6000
	s_add_u32 s14, s42, s0
	s_addc_u32 s15, s43, 0
	s_add_u32 s0, s14, 0x4000
	s_addc_u32 s1, s15, 0
	s_add_u32 s14, s14, 0x3000
	s_addc_u32 s15, s15, 0
	global_load_dwordx4 v[144:147], v3, s[40:41] offset:0
	global_load_dwordx4 v[148:151], v3, s[40:41] offset:16
	global_load_dwordx4 v[152:155], v3, s[40:41] offset:32
	global_load_dwordx4 v[156:159], v3, s[40:41] offset:48
	global_load_dwordx4 v[160:163], v3, s[0:1] offset:0
	global_load_dwordx4 v[164:167], v3, s[0:1] offset:16
	global_load_dwordx4 v[168:171], v3, s[0:1] offset:32
	global_load_dwordx4 v[172:175], v3, s[0:1] offset:48
	global_load_dwordx4 v[64:67], v3, s[14:15] offset:0
	global_load_dwordx4 v[68:71], v3, s[14:15] offset:16
	global_load_dwordx4 v[72:75], v3, s[14:15] offset:32
	global_load_dwordx4 v[76:79], v3, s[14:15] offset:48
	s_waitcnt vmcnt(0)
	v_add_f32_e32 v160, 1.0, v160
	v_add_f32_e32 v161, 1.0, v161
	v_add_f32_e32 v162, 1.0, v162
	v_add_f32_e32 v163, 1.0, v163
	v_add_f32_e32 v164, 1.0, v164
	v_add_f32_e32 v165, 1.0, v165
	v_add_f32_e32 v166, 1.0, v166
	v_add_f32_e32 v167, 1.0, v167
	v_add_f32_e32 v168, 1.0, v168
	v_add_f32_e32 v169, 1.0, v169
	v_add_f32_e32 v170, 1.0, v170
	v_add_f32_e32 v171, 1.0, v171
	v_add_f32_e32 v172, 1.0, v172
	v_add_f32_e32 v173, 1.0, v173
	v_add_f32_e32 v174, 1.0, v174
	v_add_f32_e32 v175, 1.0, v175
	v_mul_f32_e32 v48, v144, v160
	v_mul_f32_e32 v49, v145, v161
	v_mul_f32_e32 v50, v146, v162
	v_mul_f32_e32 v51, v147, v163
	v_mul_f32_e32 v52, v148, v164
	v_mul_f32_e32 v53, v149, v165
	v_mul_f32_e32 v54, v150, v166
	v_mul_f32_e32 v55, v151, v167
	v_mul_f32_e32 v56, v152, v168
	v_mul_f32_e32 v57, v153, v169
	v_mul_f32_e32 v58, v154, v170
	v_mul_f32_e32 v59, v155, v171
	v_mul_f32_e32 v60, v156, v172
	v_mul_f32_e32 v61, v157, v173
	v_mul_f32_e32 v62, v158, v174
	v_mul_f32_e32 v63, v159, v175
.Ln2_wa_ok:
	s_add_i32 s0, s46, 1
	s_cmp_lt_u32 s0, s47
	s_cbranch_scc0 .Ln2_last
	s_add_u32 s52, s50, 0x1000
	s_addc_u32 s53, s51, 0
	global_load_dwordx4 v[32:35], v3, s[52:53] offset:0
	global_load_dwordx4 v[36:39], v3, s[52:53] offset:16
	global_load_dwordx4 v[40:43], v3, s[52:53] offset:32
	global_load_dwordx4 v[44:47], v3, s[52:53] offset:48
	s_waitcnt vmcnt(4)
	s_branch .Ln2_go

.Ln2_go:
	s_lshl_b32 s0, s46, 11
	s_add_u32 s54, s36, s0
	s_addc_u32 s55, s37, 0
	v_mul_f32_e32 v8, v16, v16
	v_fmac_f32_e32 v8, v17, v17
	v_fmac_f32_e32 v8, v18, v18
	v_fmac_f32_e32 v8, v19, v19
	v_fmac_f32_e32 v8, v20, v20
	v_fmac_f32_e32 v8, v21, v21
	v_fmac_f32_e32 v8, v22, v22
	v_fmac_f32_e32 v8, v23, v23
	v_fmac_f32_e32 v8, v24, v24
	v_fmac_f32_e32 v8, v25, v25
	v_fmac_f32_e32 v8, v26, v26
	v_fmac_f32_e32 v8, v27, v27
	v_fmac_f32_e32 v8, v28, v28
	v_fmac_f32_e32 v8, v29, v29
	v_fmac_f32_e32 v8, v30, v30
	v_fmac_f32_e32 v8, v31, v31
	s_nop 1
	v_add_f32_dpp v8, v8, v8 quad_perm:[1,0,3,2] row_mask:0xf bank_mask:0xf bound_ctrl:1
	s_nop 1
	v_add_f32_dpp v8, v8, v8 quad_perm:[2,3,0,1] row_mask:0xf bank_mask:0xf bound_ctrl:1
	s_nop 1
	v_add_f32_dpp v8, v8, v8 row_half_mirror row_mask:0xf bank_mask:0xf bound_ctrl:1
	s_nop 1
	v_add_f32_dpp v8, v8, v8 row_mirror row_mask:0xf bank_mask:0xf bound_ctrl:1
	v_mov_b32_e32 v9, v8
	s_nop 1
	v_permlane16_swap_b32_e32 v8, v9
	v_add_f32_e32 v8, v8, v9
	v_mov_b32_e32 v9, v8
	s_nop 1
	v_permlane32_swap_b32_e32 v8, v9
	v_add_f32_e32 v8, v8, v9
	v_fmamk_f32 v8, v8, 0x3a800000, v1
	v_rsq_f32_e32 v11, v8
	ds_read_b128 v[96:99], v7 offset:0
	ds_read_b128 v[100:103], v7 offset:16
	ds_read_b128 v[104:107], v7 offset:32
	ds_read_b128 v[108:111], v7 offset:48
	ds_read_b128 v[112:115], v7 offset:64
	ds_read_b128 v[116:119], v7 offset:80
	ds_read_b128 v[120:123], v7 offset:96
	ds_read_b128 v[124:127], v7 offset:112
	v_mul_f32_e32 v144, v16, v11
	v_mul_f32_e32 v145, v17, v11
	v_mul_f32_e32 v146, v18, v11
	v_mul_f32_e32 v147, v19, v11
	v_mul_f32_e32 v148, v20, v11
	v_mul_f32_e32 v149, v21, v11
	v_mul_f32_e32 v150, v22, v11
	v_mul_f32_e32 v151, v23, v11
	v_mul_f32_e32 v152, v24, v11
	v_mul_f32_e32 v153, v25, v11
	v_mul_f32_e32 v154, v26, v11
	v_mul_f32_e32 v155, v27, v11
	v_mul_f32_e32 v156, v28, v11
	v_mul_f32_e32 v157, v29, v11
	v_mul_f32_e32 v158, v30, v11
	v_mul_f32_e32 v159, v31, v11
	v_fma_f32 v16, v144, v48, v64
	v_fma_f32 v17, v145, v49, v65
	v_fma_f32 v18, v146, v50, v66
	v_fma_f32 v19, v147, v51, v67
	v_fma_f32 v20, v148, v52, v68
	v_fma_f32 v21, v149, v53, v69
	v_fma_f32 v22, v150, v54, v70
	v_fma_f32 v23, v151, v55, v71
	v_fma_f32 v24, v152, v56, v72
	v_fma_f32 v25, v153, v57, v73
	v_fma_f32 v26, v154, v58, v74
	v_fma_f32 v27, v155, v59, v75
	v_fma_f32 v28, v156, v60, v76
	v_fma_f32 v29, v157, v61, v77
	v_fma_f32 v30, v158, v62, v78
	v_fma_f32 v31, v159, v63, v79
	v_cvt_pk_bf16_f32 v176, v16, v17
	v_cvt_pk_bf16_f32 v177, v18, v19
	v_cvt_pk_bf16_f32 v178, v20, v21
	v_cvt_pk_bf16_f32 v179, v22, v23
	v_cvt_pk_bf16_f32 v180, v24, v25
	v_cvt_pk_bf16_f32 v181, v26, v27
	v_cvt_pk_bf16_f32 v182, v28, v29
	v_cvt_pk_bf16_f32 v183, v30, v31
	global_store_dwordx4 v4, v[176:179], s[54:55]
	global_store_dwordx4 v4, v[180:183], s[54:55] offset:16
	s_waitcnt lgkmcnt(4)
	ds_read_b128 v[128:131], v7 offset:128
	ds_read_b128 v[132:135], v7 offset:144
	ds_read_b128 v[136:139], v7 offset:160
	ds_read_b128 v[140:143], v7 offset:176
	v_pk_mul_f32 v[80:81], v[16:17], v[96:97] op_sel:[0,0] op_sel_hi:[0,1]
	v_pk_mul_f32 v[82:83], v[16:17], v[98:99] op_sel:[0,0] op_sel_hi:[0,1]
	v_pk_mul_f32 v[84:85], v[16:17], v[100:101] op_sel:[0,0] op_sel_hi:[0,1]
	v_pk_mul_f32 v[86:87], v[16:17], v[102:103] op_sel:[0,0] op_sel_hi:[0,1]
	v_pk_mul_f32 v[88:89], v[16:17], v[104:105] op_sel:[0,0] op_sel_hi:[0,1]
	v_pk_mul_f32 v[90:91], v[16:17], v[106:107] op_sel:[0,0] op_sel_hi:[0,1]
	v_pk_mul_f32 v[92:93], v[16:17], v[108:109] op_sel:[0,0] op_sel_hi:[0,1]
	v_pk_mul_f32 v[94:95], v[16:17], v[110:111] op_sel:[0,0] op_sel_hi:[0,1]
	s_waitcnt lgkmcnt(4)
	ds_read_b128 v[96:99], v7 offset:192
	ds_read_b128 v[100:103], v7 offset:208
	ds_read_b128 v[104:107], v7 offset:224
	ds_read_b128 v[108:111], v7 offset:240
	v_pk_fma_f32 v[80:81], v[16:17], v[112:113], v[80:81] op_sel:[1,0,0] op_sel_hi:[1,1,1]
	v_pk_fma_f32 v[82:83], v[16:17], v[114:115], v[82:83] op_sel:[1,0,0] op_sel_hi:[1,1,1]
	v_pk_fma_f32 v[84:85], v[16:17], v[116:117], v[84:85] op_sel:[1,0,0] op_sel_hi:[1,1,1]
	v_pk_fma_f32 v[86:87], v[16:17], v[118:119], v[86:87] op_sel:[1,0,0] op_sel_hi:[1,1,1]
	v_pk_fma_f32 v[88:89], v[16:17], v[120:121], v[88:89] op_sel:[1,0,0] op_sel_hi:[1,1,1]
	v_pk_fma_f32 v[90:91], v[16:17], v[122:123], v[90:91] op_sel:[1,0,0] op_sel_hi:[1,1,1]
	v_pk_fma_f32 v[92:93], v[16:17], v[124:125], v[92:93] op_sel:[1,0,0] op_sel_hi:[1,1,1]
	v_pk_fma_f32 v[94:95], v[16:17], v[126:127], v[94:95] op_sel:[1,0,0] op_sel_hi:[1,1,1]
	s_waitcnt lgkmcnt(4)
	ds_read_b128 v[112:115], v7 offset:256
	ds_read_b128 v[116:119], v7 offset:272
	ds_read_b128 v[120:123], v7 offset:288
	ds_read_b128 v[124:127], v7 offset:304
	v_pk_fma_f32 v[80:81], v[18:19], v[128:129], v[80:81] op_sel:[0,0,0] op_sel_hi:[0,1,1]
	v_pk_fma_f32 v[82:83], v[18:19], v[130:131], v[82:83] op_sel:[0,0,0] op_sel_hi:[0,1,1]
	v_pk_fma_f32 v[84:85], v[18:19], v[132:133], v[84:85] op_sel:[0,0,0] op_sel_hi:[0,1,1]
	v_pk_fma_f32 v[86:87], v[18:19], v[134:135], v[86:87] op_sel:[0,0,0] op_sel_hi:[0,1,1]
	v_pk_fma_f32 v[88:89], v[18:19], v[136:137], v[88:89] op_sel:[0,0,0] op_sel_hi:[0,1,1]
	v_pk_fma_f32 v[90:91], v[18:19], v[138:139], v[90:91] op_sel:[0,0,0] op_sel_hi:[0,1,1]
	v_pk_fma_f32 v[92:93], v[18:19], v[140:141], v[92:93] op_sel:[0,0,0] op_sel_hi:[0,1,1]
	v_pk_fma_f32 v[94:95], v[18:19], v[142:143], v[94:95] op_sel:[0,0,0] op_sel_hi:[0,1,1]
	s_waitcnt lgkmcnt(4)
	ds_read_b128 v[128:131], v7 offset:320
	ds_read_b128 v[132:135], v7 offset:336
	ds_read_b128 v[136:139], v7 offset:352
	ds_read_b128 v[140:143], v7 offset:368
	v_pk_fma_f32 v[80:81], v[18:19], v[96:97], v[80:81] op_sel:[1,0,0] op_sel_hi:[1,1,1]
	v_pk_fma_f32 v[82:83], v[18:19], v[98:99], v[82:83] op_sel:[1,0,0] op_sel_hi:[1,1,1]
	v_pk_fma_f32 v[84:85], v[18:19], v[100:101], v[84:85] op_sel:[1,0,0] op_sel_hi:[1,1,1]
	v_pk_fma_f32 v[86:87], v[18:19], v[102:103], v[86:87] op_sel:[1,0,0] op_sel_hi:[1,1,1]
	v_pk_fma_f32 v[88:89], v[18:19], v[104:105], v[88:89] op_sel:[1,0,0] op_sel_hi:[1,1,1]
	v_pk_fma_f32 v[90:91], v[18:19], v[106:107], v[90:91] op_sel:[1,0,0] op_sel_hi:[1,1,1]
	v_pk_fma_f32 v[92:93], v[18:19], v[108:109], v[92:93] op_sel:[1,0,0] op_sel_hi:[1,1,1]
	v_pk_fma_f32 v[94:95], v[18:19], v[110:111], v[94:95] op_sel:[1,0,0] op_sel_hi:[1,1,1]
	s_waitcnt lgkmcnt(4)
	ds_read_b128 v[96:99], v7 offset:384
	ds_read_b128 v[100:103], v7 offset:400
	ds_read_b128 v[104:107], v7 offset:416
	ds_read_b128 v[108:111], v7 offset:432
	v_pk_fma_f32 v[80:81], v[20:21], v[112:113], v[80:81] op_sel:[0,0,0] op_sel_hi:[0,1,1]
	v_pk_fma_f32 v[82:83], v[20:21], v[114:115], v[82:83] op_sel:[0,0,0] op_sel_hi:[0,1,1]
	v_pk_fma_f32 v[84:85], v[20:21], v[116:117], v[84:85] op_sel:[0,0,0] op_sel_hi:[0,1,1]
	v_pk_fma_f32 v[86:87], v[20:21], v[118:119], v[86:87] op_sel:[0,0,0] op_sel_hi:[0,1,1]
	v_pk_fma_f32 v[88:89], v[20:21], v[120:121], v[88:89] op_sel:[0,0,0] op_sel_hi:[0,1,1]
	v_pk_fma_f32 v[90:91], v[20:21], v[122:123], v[90:91] op_sel:[0,0,0] op_sel_hi:[0,1,1]
	v_pk_fma_f32 v[92:93], v[20:21], v[124:125], v[92:93] op_sel:[0,0,0] op_sel_hi:[0,1,1]
	v_pk_fma_f32 v[94:95], v[20:21], v[126:127], v[94:95] op_sel:[0,0,0] op_sel_hi:[0,1,1]
	s_waitcnt lgkmcnt(4)
	ds_read_b128 v[112:115], v7 offset:448
	ds_read_b128 v[116:119], v7 offset:464
	ds_read_b128 v[120:123], v7 offset:480
	ds_read_b128 v[124:127], v7 offset:496
	v_pk_fma_f32 v[80:81], v[20:21], v[128:129], v[80:81] op_sel:[1,0,0] op_sel_hi:[1,1,1]
	v_pk_fma_f32 v[82:83], v[20:21], v[130:131], v[82:83] op_sel:[1,0,0] op_sel_hi:[1,1,1]
	v_pk_fma_f32 v[84:85], v[20:21], v[132:133], v[84:85] op_sel:[1,0,0] op_sel_hi:[1,1,1]
	v_pk_fma_f32 v[86:87], v[20:21], v[134:135], v[86:87] op_sel:[1,0,0] op_sel_hi:[1,1,1]
	v_pk_fma_f32 v[88:89], v[20:21], v[136:137], v[88:89] op_sel:[1,0,0] op_sel_hi:[1,1,1]
	v_pk_fma_f32 v[90:91], v[20:21], v[138:139], v[90:91] op_sel:[1,0,0] op_sel_hi:[1,1,1]
	v_pk_fma_f32 v[92:93], v[20:21], v[140:141], v[92:93] op_sel:[1,0,0] op_sel_hi:[1,1,1]
	v_pk_fma_f32 v[94:95], v[20:21], v[142:143], v[94:95] op_sel:[1,0,0] op_sel_hi:[1,1,1]
	s_waitcnt lgkmcnt(4)
	ds_read_b128 v[128:131], v7 offset:512
	ds_read_b128 v[132:135], v7 offset:528
	ds_read_b128 v[136:139], v7 offset:544
	ds_read_b128 v[140:143], v7 offset:560
	v_pk_fma_f32 v[80:81], v[22:23], v[96:97], v[80:81] op_sel:[0,0,0] op_sel_hi:[0,1,1]
	v_pk_fma_f32 v[82:83], v[22:23], v[98:99], v[82:83] op_sel:[0,0,0] op_sel_hi:[0,1,1]
	v_pk_fma_f32 v[84:85], v[22:23], v[100:101], v[84:85] op_sel:[0,0,0] op_sel_hi:[0,1,1]
	v_pk_fma_f32 v[86:87], v[22:23], v[102:103], v[86:87] op_sel:[0,0,0] op_sel_hi:[0,1,1]
	v_pk_fma_f32 v[88:89], v[22:23], v[104:105], v[88:89] op_sel:[0,0,0] op_sel_hi:[0,1,1]
	v_pk_fma_f32 v[90:91], v[22:23], v[106:107], v[90:91] op_sel:[0,0,0] op_sel_hi:[0,1,1]
	v_pk_fma_f32 v[92:93], v[22:23], v[108:109], v[92:93] op_sel:[0,0,0] op_sel_hi:[0,1,1]
	v_pk_fma_f32 v[94:95], v[22:23], v[110:111], v[94:95] op_sel:[0,0,0] op_sel_hi:[0,1,1]
	s_waitcnt lgkmcnt(4)
	ds_read_b128 v[96:99], v7 offset:576
	ds_read_b128 v[100:103], v7 offset:592
	ds_read_b128 v[104:107], v7 offset:608
	ds_read_b128 v[108:111], v7 offset:624
	v_pk_fma_f32 v[80:81], v[22:23], v[112:113], v[80:81] op_sel:[1,0,0] op_sel_hi:[1,1,1]
	v_pk_fma_f32 v[82:83], v[22:23], v[114:115], v[82:83] op_sel:[1,0,0] op_sel_hi:[1,1,1]
	v_pk_fma_f32 v[84:85], v[22:23], v[116:117], v[84:85] op_sel:[1,0,0] op_sel_hi:[1,1,1]
	v_pk_fma_f32 v[86:87], v[22:23], v[118:119], v[86:87] op_sel:[1,0,0] op_sel_hi:[1,1,1]
	v_pk_fma_f32 v[88:89], v[22:23], v[120:121], v[88:89] op_sel:[1,0,0] op_sel_hi:[1,1,1]
	v_pk_fma_f32 v[90:91], v[22:23], v[122:123], v[90:91] op_sel:[1,0,0] op_sel_hi:[1,1,1]
	v_pk_fma_f32 v[92:93], v[22:23], v[124:125], v[92:93] op_sel:[1,0,0] op_sel_hi:[1,1,1]
	v_pk_fma_f32 v[94:95], v[22:23], v[126:127], v[94:95] op_sel:[1,0,0] op_sel_hi:[1,1,1]
	s_waitcnt lgkmcnt(4)
	ds_read_b128 v[112:115], v7 offset:640
	ds_read_b128 v[116:119], v7 offset:656
	ds_read_b128 v[120:123], v7 offset:672
	ds_read_b128 v[124:127], v7 offset:688
	v_pk_fma_f32 v[80:81], v[24:25], v[128:129], v[80:81] op_sel:[0,0,0] op_sel_hi:[0,1,1]
	v_pk_fma_f32 v[82:83], v[24:25], v[130:131], v[82:83] op_sel:[0,0,0] op_sel_hi:[0,1,1]
	v_pk_fma_f32 v[84:85], v[24:25], v[132:133], v[84:85] op_sel:[0,0,0] op_sel_hi:[0,1,1]
	v_pk_fma_f32 v[86:87], v[24:25], v[134:135], v[86:87] op_sel:[0,0,0] op_sel_hi:[0,1,1]
	v_pk_fma_f32 v[88:89], v[24:25], v[136:137], v[88:89] op_sel:[0,0,0] op_sel_hi:[0,1,1]
	v_pk_fma_f32 v[90:91], v[24:25], v[138:139], v[90:91] op_sel:[0,0,0] op_sel_hi:[0,1,1]
	v_pk_fma_f32 v[92:93], v[24:25], v[140:141], v[92:93] op_sel:[0,0,0] op_sel_hi:[0,1,1]
	v_pk_fma_f32 v[94:95], v[24:25], v[142:143], v[94:95] op_sel:[0,0,0] op_sel_hi:[0,1,1]
	s_waitcnt lgkmcnt(4)
	ds_read_b128 v[128:131], v7 offset:704
	ds_read_b128 v[132:135], v7 offset:720
	ds_read_b128 v[136:139], v7 offset:736
	ds_read_b128 v[140:143], v7 offset:752
	v_pk_fma_f32 v[80:81], v[24:25], v[96:97], v[80:81] op_sel:[1,0,0] op_sel_hi:[1,1,1]
	v_pk_fma_f32 v[82:83], v[24:25], v[98:99], v[82:83] op_sel:[1,0,0] op_sel_hi:[1,1,1]
	v_pk_fma_f32 v[84:85], v[24:25], v[100:101], v[84:85] op_sel:[1,0,0] op_sel_hi:[1,1,1]
	v_pk_fma_f32 v[86:87], v[24:25], v[102:103], v[86:87] op_sel:[1,0,0] op_sel_hi:[1,1,1]
	v_pk_fma_f32 v[88:89], v[24:25], v[104:105], v[88:89] op_sel:[1,0,0] op_sel_hi:[1,1,1]
	v_pk_fma_f32 v[90:91], v[24:25], v[106:107], v[90:91] op_sel:[1,0,0] op_sel_hi:[1,1,1]
	v_pk_fma_f32 v[92:93], v[24:25], v[108:109], v[92:93] op_sel:[1,0,0] op_sel_hi:[1,1,1]
	v_pk_fma_f32 v[94:95], v[24:25], v[110:111], v[94:95] op_sel:[1,0,0] op_sel_hi:[1,1,1]
	s_waitcnt lgkmcnt(4)
	ds_read_b128 v[96:99], v7 offset:768
	ds_read_b128 v[100:103], v7 offset:784
	ds_read_b128 v[104:107], v7 offset:800
	ds_read_b128 v[108:111], v7 offset:816
	v_pk_fma_f32 v[80:81], v[26:27], v[112:113], v[80:81] op_sel:[0,0,0] op_sel_hi:[0,1,1]
	v_pk_fma_f32 v[82:83], v[26:27], v[114:115], v[82:83] op_sel:[0,0,0] op_sel_hi:[0,1,1]
	v_pk_fma_f32 v[84:85], v[26:27], v[116:117], v[84:85] op_sel:[0,0,0] op_sel_hi:[0,1,1]
	v_pk_fma_f32 v[86:87], v[26:27], v[118:119], v[86:87] op_sel:[0,0,0] op_sel_hi:[0,1,1]
	v_pk_fma_f32 v[88:89], v[26:27], v[120:121], v[88:89] op_sel:[0,0,0] op_sel_hi:[0,1,1]
	v_pk_fma_f32 v[90:91], v[26:27], v[122:123], v[90:91] op_sel:[0,0,0] op_sel_hi:[0,1,1]
	v_pk_fma_f32 v[92:93], v[26:27], v[124:125], v[92:93] op_sel:[0,0,0] op_sel_hi:[0,1,1]
	v_pk_fma_f32 v[94:95], v[26:27], v[126:127], v[94:95] op_sel:[0,0,0] op_sel_hi:[0,1,1]
	s_waitcnt lgkmcnt(4)
	ds_read_b128 v[112:115], v7 offset:832
	ds_read_b128 v[116:119], v7 offset:848
	ds_read_b128 v[120:123], v7 offset:864
	ds_read_b128 v[124:127], v7 offset:880
	v_pk_fma_f32 v[80:81], v[26:27], v[128:129], v[80:81] op_sel:[1,0,0] op_sel_hi:[1,1,1]
	v_pk_fma_f32 v[82:83], v[26:27], v[130:131], v[82:83] op_sel:[1,0,0] op_sel_hi:[1,1,1]
	v_pk_fma_f32 v[84:85], v[26:27], v[132:133], v[84:85] op_sel:[1,0,0] op_sel_hi:[1,1,1]
	v_pk_fma_f32 v[86:87], v[26:27], v[134:135], v[86:87] op_sel:[1,0,0] op_sel_hi:[1,1,1]
	v_pk_fma_f32 v[88:89], v[26:27], v[136:137], v[88:89] op_sel:[1,0,0] op_sel_hi:[1,1,1]
	v_pk_fma_f32 v[90:91], v[26:27], v[138:139], v[90:91] op_sel:[1,0,0] op_sel_hi:[1,1,1]
	v_pk_fma_f32 v[92:93], v[26:27], v[140:141], v[92:93] op_sel:[1,0,0] op_sel_hi:[1,1,1]
	v_pk_fma_f32 v[94:95], v[26:27], v[142:143], v[94:95] op_sel:[1,0,0] op_sel_hi:[1,1,1]
	s_waitcnt lgkmcnt(4)
	ds_read_b128 v[128:131], v7 offset:896
	ds_read_b128 v[132:135], v7 offset:912
	ds_read_b128 v[136:139], v7 offset:928
	ds_read_b128 v[140:143], v7 offset:944
	v_pk_fma_f32 v[80:81], v[28:29], v[96:97], v[80:81] op_sel:[0,0,0] op_sel_hi:[0,1,1]
	v_pk_fma_f32 v[82:83], v[28:29], v[98:99], v[82:83] op_sel:[0,0,0] op_sel_hi:[0,1,1]
	v_pk_fma_f32 v[84:85], v[28:29], v[100:101], v[84:85] op_sel:[0,0,0] op_sel_hi:[0,1,1]
	v_pk_fma_f32 v[86:87], v[28:29], v[102:103], v[86:87] op_sel:[0,0,0] op_sel_hi:[0,1,1]
	v_pk_fma_f32 v[88:89], v[28:29], v[104:105], v[88:89] op_sel:[0,0,0] op_sel_hi:[0,1,1]
	v_pk_fma_f32 v[90:91], v[28:29], v[106:107], v[90:91] op_sel:[0,0,0] op_sel_hi:[0,1,1]
	v_pk_fma_f32 v[92:93], v[28:29], v[108:109], v[92:93] op_sel:[0,0,0] op_sel_hi:[0,1,1]
	v_pk_fma_f32 v[94:95], v[28:29], v[110:111], v[94:95] op_sel:[0,0,0] op_sel_hi:[0,1,1]
	s_waitcnt lgkmcnt(4)
	ds_read_b128 v[96:99], v7 offset:960
	ds_read_b128 v[100:103], v7 offset:976
	ds_read_b128 v[104:107], v7 offset:992
	ds_read_b128 v[108:111], v7 offset:1008
	v_pk_fma_f32 v[80:81], v[28:29], v[112:113], v[80:81] op_sel:[1,0,0] op_sel_hi:[1,1,1]
	v_pk_fma_f32 v[82:83], v[28:29], v[114:115], v[82:83] op_sel:[1,0,0] op_sel_hi:[1,1,1]
	v_pk_fma_f32 v[84:85], v[28:29], v[116:117], v[84:85] op_sel:[1,0,0] op_sel_hi:[1,1,1]
	v_pk_fma_f32 v[86:87], v[28:29], v[118:119], v[86:87] op_sel:[1,0,0] op_sel_hi:[1,1,1]
	v_pk_fma_f32 v[88:89], v[28:29], v[120:121], v[88:89] op_sel:[1,0,0] op_sel_hi:[1,1,1]
	v_pk_fma_f32 v[90:91], v[28:29], v[122:123], v[90:91] op_sel:[1,0,0] op_sel_hi:[1,1,1]
	v_pk_fma_f32 v[92:93], v[28:29], v[124:125], v[92:93] op_sel:[1,0,0] op_sel_hi:[1,1,1]
	v_pk_fma_f32 v[94:95], v[28:29], v[126:127], v[94:95] op_sel:[1,0,0] op_sel_hi:[1,1,1]
	s_waitcnt lgkmcnt(4)
	v_pk_fma_f32 v[80:81], v[30:31], v[128:129], v[80:81] op_sel:[0,0,0] op_sel_hi:[0,1,1]
	v_pk_fma_f32 v[82:83], v[30:31], v[130:131], v[82:83] op_sel:[0,0,0] op_sel_hi:[0,1,1]
	v_pk_fma_f32 v[84:85], v[30:31], v[132:133], v[84:85] op_sel:[0,0,0] op_sel_hi:[0,1,1]
	v_pk_fma_f32 v[86:87], v[30:31], v[134:135], v[86:87] op_sel:[0,0,0] op_sel_hi:[0,1,1]
	v_pk_fma_f32 v[88:89], v[30:31], v[136:137], v[88:89] op_sel:[0,0,0] op_sel_hi:[0,1,1]
	v_pk_fma_f32 v[90:91], v[30:31], v[138:139], v[90:91] op_sel:[0,0,0] op_sel_hi:[0,1,1]
	v_pk_fma_f32 v[92:93], v[30:31], v[140:141], v[92:93] op_sel:[0,0,0] op_sel_hi:[0,1,1]
	v_pk_fma_f32 v[94:95], v[30:31], v[142:143], v[94:95] op_sel:[0,0,0] op_sel_hi:[0,1,1]
	s_waitcnt lgkmcnt(0)
	v_pk_fma_f32 v[80:81], v[30:31], v[96:97], v[80:81] op_sel:[1,0,0] op_sel_hi:[1,1,1]
	v_pk_fma_f32 v[82:83], v[30:31], v[98:99], v[82:83] op_sel:[1,0,0] op_sel_hi:[1,1,1]
	v_pk_fma_f32 v[84:85], v[30:31], v[100:101], v[84:85] op_sel:[1,0,0] op_sel_hi:[1,1,1]
	v_pk_fma_f32 v[86:87], v[30:31], v[102:103], v[86:87] op_sel:[1,0,0] op_sel_hi:[1,1,1]
	v_pk_fma_f32 v[88:89], v[30:31], v[104:105], v[88:89] op_sel:[1,0,0] op_sel_hi:[1,1,1]
	v_pk_fma_f32 v[90:91], v[30:31], v[106:107], v[90:91] op_sel:[1,0,0] op_sel_hi:[1,1,1]
	v_pk_fma_f32 v[92:93], v[30:31], v[108:109], v[92:93] op_sel:[1,0,0] op_sel_hi:[1,1,1]
	v_pk_fma_f32 v[94:95], v[30:31], v[110:111], v[94:95] op_sel:[1,0,0] op_sel_hi:[1,1,1]
	v_cndmask_b32_e64 v144, v80, v88, s[58:59]
	v_cndmask_b32_e64 v152, v88, v80, s[58:59]
	v_cndmask_b32_e64 v145, v81, v89, s[58:59]
	v_cndmask_b32_e64 v153, v89, v81, s[58:59]
	v_cndmask_b32_e64 v146, v82, v90, s[58:59]
	v_cndmask_b32_e64 v154, v90, v82, s[58:59]
	v_cndmask_b32_e64 v147, v83, v91, s[58:59]
	v_cndmask_b32_e64 v155, v91, v83, s[58:59]
	v_cndmask_b32_e64 v148, v84, v92, s[58:59]
	v_cndmask_b32_e64 v156, v92, v84, s[58:59]
	v_cndmask_b32_e64 v149, v85, v93, s[58:59]
	v_cndmask_b32_e64 v157, v93, v85, s[58:59]
	v_cndmask_b32_e64 v150, v86, v94, s[58:59]
	v_cndmask_b32_e64 v158, v94, v86, s[58:59]
	v_cndmask_b32_e64 v151, v87, v95, s[58:59]
	v_cndmask_b32_e64 v159, v95, v87, s[58:59]
	v_add_f32_dpp v160, v152, v144 quad_perm:[1,0,3,2] row_mask:0xf bank_mask:0xf bound_ctrl:1
	v_add_f32_dpp v161, v153, v145 quad_perm:[1,0,3,2] row_mask:0xf bank_mask:0xf bound_ctrl:1
	v_add_f32_dpp v162, v154, v146 quad_perm:[1,0,3,2] row_mask:0xf bank_mask:0xf bound_ctrl:1
	v_add_f32_dpp v163, v155, v147 quad_perm:[1,0,3,2] row_mask:0xf bank_mask:0xf bound_ctrl:1
	v_add_f32_dpp v164, v156, v148 quad_perm:[1,0,3,2] row_mask:0xf bank_mask:0xf bound_ctrl:1
	v_add_f32_dpp v165, v157, v149 quad_perm:[1,0,3,2] row_mask:0xf bank_mask:0xf bound_ctrl:1
	v_add_f32_dpp v166, v158, v150 quad_perm:[1,0,3,2] row_mask:0xf bank_mask:0xf bound_ctrl:1
	v_add_f32_dpp v167, v159, v151 quad_perm:[1,0,3,2] row_mask:0xf bank_mask:0xf bound_ctrl:1
	v_cndmask_b32_e64 v144, v160, v164, s[60:61]
	v_cndmask_b32_e64 v152, v164, v160, s[60:61]
	v_cndmask_b32_e64 v145, v161, v165, s[60:61]
	v_cndmask_b32_e64 v153, v165, v161, s[60:61]
	v_cndmask_b32_e64 v146, v162, v166, s[60:61]
	v_cndmask_b32_e64 v154, v166, v162, s[60:61]
	v_cndmask_b32_e64 v147, v163, v167, s[60:61]
	v_cndmask_b32_e64 v155, v167, v163, s[60:61]
	v_add_f32_dpp v80, v152, v144 quad_perm:[2,3,0,1] row_mask:0xf bank_mask:0xf bound_ctrl:1
	v_add_f32_dpp v81, v153, v145 quad_perm:[2,3,0,1] row_mask:0xf bank_mask:0xf bound_ctrl:1
	v_add_f32_dpp v82, v154, v146 quad_perm:[2,3,0,1] row_mask:0xf bank_mask:0xf bound_ctrl:1
	v_add_f32_dpp v83, v155, v147 quad_perm:[2,3,0,1] row_mask:0xf bank_mask:0xf bound_ctrl:1
	v_cndmask_b32_e64 v144, v80, v82, s[62:63]
	v_cndmask_b32_e64 v152, v82, v80, s[62:63]
	v_cndmask_b32_e64 v145, v81, v83, s[62:63]
	v_cndmask_b32_e64 v153, v83, v81, s[62:63]
	s_nop 1
	v_mov_b32_dpp v152, v152 quad_perm:[3,2,1,0] row_mask:0xf bank_mask:0xf bound_ctrl:1
	s_nop 1
	v_mov_b32_dpp v153, v153 quad_perm:[3,2,1,0] row_mask:0xf bank_mask:0xf bound_ctrl:1
	s_nop 1
	v_add_f32_dpp v160, v152, v144 row_half_mirror row_mask:0xf bank_mask:0xf bound_ctrl:1
	s_nop 1
	v_add_f32_dpp v161, v153, v145 row_half_mirror row_mask:0xf bank_mask:0xf bound_ctrl:1
	v_cndmask_b32_e64 v144, v160, v161, s[64:65]
	v_cndmask_b32_e64 v152, v161, v160, s[64:65]
	s_nop 1
	v_mov_b32_dpp v152, v152 row_half_mirror row_mask:0xf bank_mask:0xf bound_ctrl:1
	s_nop 1
	v_add_f32_dpp v80, v152, v144 row_mirror row_mask:0xf bank_mask:0xf bound_ctrl:1
	v_mov_b32_e32 v9, v80
	s_nop 1
	v_permlane16_swap_b32_e32 v80, v9
	v_add_f32_e32 v80, v80, v9
	v_mov_b32_e32 v9, v80
	s_nop 1
	v_permlane32_swap_b32_e32 v80, v9
	v_add_f32_e32 v80, v80, v9
	v_mov_b32_e32 v10, v80
	s_nop 1
	v_max_f32_dpp v10, v10, v10 quad_perm:[1,0,3,2] row_mask:0xf bank_mask:0xf bound_ctrl:1
	s_nop 1
	v_max_f32_dpp v10, v10, v10 quad_perm:[2,3,0,1] row_mask:0xf bank_mask:0xf bound_ctrl:1
	s_nop 1
	v_max_f32_dpp v10, v10, v10 row_half_mirror row_mask:0xf bank_mask:0xf bound_ctrl:1
	s_nop 1
	v_max_f32_dpp v10, v10, v10 row_mirror row_mask:0xf bank_mask:0xf bound_ctrl:1
	v_sub_f32_e32 v9, v80, v10
	v_mul_f32_e32 v9, 0x3fb8aa3b, v9
	v_exp_f32_e32 v9, v9
	s_nop 0
	v_mov_b32_e32 v10, v9
	s_nop 1
	v_add_f32_dpp v10, v10, v10 quad_perm:[1,0,3,2] row_mask:0xf bank_mask:0xf bound_ctrl:1
	s_nop 1
	v_add_f32_dpp v10, v10, v10 quad_perm:[2,3,0,1] row_mask:0xf bank_mask:0xf bound_ctrl:1
	s_nop 1
	v_add_f32_dpp v10, v10, v10 row_half_mirror row_mask:0xf bank_mask:0xf bound_ctrl:1
	s_nop 1
	v_add_f32_dpp v10, v10, v10 row_mirror row_mask:0xf bank_mask:0xf bound_ctrl:1
	v_rcp_f32_e32 v10, v10
	s_nop 0
	v_mul_f32_e32 v9, v9, v10
	s_mov_b64 exec, s[66:67]
	s_cmp_lt_u32 s46, 0x4000
	s_cbranch_scc0 .Ln2_ctx
	s_lshr_b32 s0, s46, 13
	s_lshl_b32 s0, s0, 19
	s_and_b32 s1, s46, 0x1fff
	s_lshl_b32 s1, s1, 2
	s_add_u32 s0, s0, s1
	s_add_u32 s56, s38, s0
	s_addc_u32 s57, s39, 0
	global_store_dword v5, v9, s[56:57]
	s_branch .Ln2_affdone
.Ln2_ctx:
	s_sub_u32 s0, s46, 0x4000
	s_lshr_b32 s1, s0, 8
	s_lshl_b32 s1, s1, 14
	s_and_b32 s0, s0, 0xff
	s_lshl_b32 s0, s0, 2
	s_add_u32 s0, s0, s1
	s_add_u32 s0, s0, 0x100000
	s_add_u32 s56, s38, s0
	s_addc_u32 s57, s39, 0
	global_store_dword v6, v9, s[56:57]
.Ln2_affdone:
	s_mov_b64 exec, -1
	s_add_i32 s46, s46, 1
	s_cmp_lt_u32 s46, s47
	s_cbranch_scc0 .Ln2_done
	s_mov_b64 s[50:51], s[52:53]
	s_waitcnt vmcnt(3)
	v_mov_b32_e32 v16, v32
	v_mov_b32_e32 v17, v33
	v_mov_b32_e32 v18, v34
	v_mov_b32_e32 v19, v35
	v_mov_b32_e32 v20, v36
	v_mov_b32_e32 v21, v37
	v_mov_b32_e32 v22, v38
	v_mov_b32_e32 v23, v39
	v_mov_b32_e32 v24, v40
	v_mov_b32_e32 v25, v41
	v_mov_b32_e32 v26, v42
	v_mov_b32_e32 v27, v43
	v_mov_b32_e32 v28, v44
	v_mov_b32_e32 v29, v45
	v_mov_b32_e32 v30, v46
	v_mov_b32_e32 v31, v47
	s_branch .Ln2_row
.Ln2_done:
	s_mov_b64 s[30:31], exec
.LBB0_1402:
	s_or_b64 exec, exec, s[30:31]
	s_add_i32 s9, s3, 8
	s_cmp_ge_i32 s9, s75
	s_cbranch_scc1 .LBB0_1456
	s_waitcnt vmcnt(0)
	s_barrier
	s_mov_b64 s[0:1], exec
	v_readlane_b32 s14, v254, 1
	v_readlane_b32 s15, v254, 2
	s_and_b64 s[14:15], s[0:1], s[14:15]
	s_mov_b64 exec, s[14:15]
	s_cbranch_execz .LBB0_1455
	s_waitcnt vmcnt(0) expcnt(0) lgkmcnt(0)
	ds_read_b32 v4, v195
	ds_read_b32 v2, v195 offset:4
	s_waitcnt lgkmcnt(1)
	v_cmp_ne_u32_e32 vcc, 0, v4
	s_cbranch_vccnz .LBB0_1419
	v_readlane_b32 s30, v254, 3
	v_readlane_b32 s31, v254, 4
	s_load_dwordx2 s[14:15], s[30:31], 0x4
	s_mov_b32 s36, 1
	s_waitcnt lgkmcnt(0)
	s_mul_i32 s29, s14, s29
	s_mul_i32 s29, s29, s15
	s_branch .LBB0_1407
